# v039 + diff MFMA segment PV-first (fragments read after the barrier), splat and K address adds spread over the PV gaps
# baseline (speedup 1.0000x reference)
; #define PK4(P, BASE, OUT) do { u32x4 w = {cvtpk(P[BASE + 0], P[BASE + 1]), cvtpk(P[BASE + 2], P[BASE + 3]), cvtpk(P[BASE + 4], P[BASE + 5]), cvtpk(P[BASE + 6], P[BASE + 7])}; \
;     OUT = *reinterpret_cast<bf16x8*>(&w); } while (0)
; __device__ __forceinline__ void smax_tile(f32x16& p0, f32x16& p1, float& mhat, float& l_reg, f32x16 (&o)[4], float* al_l, const bool first, int r32, int hi,
;                                           bf16x8& pa0, bf16x8& pa1, bf16x8& pa2, bf16x8& pa3) {
;     ...
; #pragma unroll
;     for (int r = 0; r < 16; ++r) p0[r] = __builtin_amdgcn_exp2f(p0[r]);
; #pragma unroll
;     for (int r = 0; r < 16; ++r) p1[r] = __builtin_amdgcn_exp2f(p1[r]);
;     float ps = p0[0];
; #pragma unroll
;     for (int r = 1; r < 16; ++r) ps += p0[r];
; #pragma unroll
;     for (int r = 0; r < 16; ++r) ps += p1[r];
;     { auto rr = __builtin_amdgcn_permlane32_swap(__float_as_uint(ps), __float_as_uint(ps), false, false); ps = __uint_as_float(rr[0]) + __uint_as_float(rr[1]); }
;     l_reg += ps;
;     ...
;     PK4(p0, 0, pa0); PK4(p0, 8, pa1); PK4(p1, 0, pa2); PK4(p1, 8, pa3);
.LBB0_651:
	v_exp_f32_e32 v96, v96
	v_exp_f32_e32 v97, v97
	v_exp_f32_e32 v98, v98
	v_exp_f32_e32 v99, v99
	v_exp_f32_e32 v100, v100
	v_exp_f32_e32 v101, v101
	v_add_f32_e32 v128, v96, v97
	v_exp_f32_e32 v102, v102
	v_add_f32_e32 v128, v98, v128
	v_exp_f32_e32 v103, v103
	v_add_f32_e32 v128, v99, v128
	v_exp_f32_e32 v104, v104
	v_add_f32_e32 v128, v100, v128
	v_exp_f32_e32 v105, v105
	v_add_f32_e32 v128, v101, v128
	v_exp_f32_e32 v106, v106
	v_add_f32_e32 v128, v102, v128
	v_exp_f32_e32 v107, v107
	v_add_f32_e32 v128, v103, v128
	v_exp_f32_e32 v108, v108
	v_add_f32_e32 v128, v104, v128
	v_exp_f32_e32 v109, v109
	v_add_f32_e32 v128, v105, v128
	v_exp_f32_e32 v110, v110
	v_add_f32_e32 v128, v106, v128
	v_exp_f32_e32 v111, v111
	v_add_f32_e32 v128, v107, v128
	v_exp_f32_e32 v80, v80
	v_add_f32_e32 v128, v108, v128
	v_exp_f32_e32 v81, v81
	v_add_f32_e32 v128, v109, v128
	v_exp_f32_e32 v82, v82
	v_add_f32_e32 v128, v110, v128
	v_exp_f32_e32 v83, v83
	v_add_f32_e32 v128, v111, v128
	v_exp_f32_e32 v84, v84
	v_add_f32_e32 v128, v80, v128
	v_exp_f32_e32 v85, v85
	v_add_f32_e32 v128, v81, v128
	v_exp_f32_e32 v86, v86
	v_add_f32_e32 v128, v82, v128
	v_exp_f32_e32 v87, v87
	v_add_f32_e32 v128, v83, v128
	v_exp_f32_e32 v88, v88
	v_add_f32_e32 v128, v84, v128
	v_exp_f32_e32 v89, v89
	v_add_f32_e32 v128, v85, v128
	v_exp_f32_e32 v90, v90
	v_add_f32_e32 v128, v86, v128
	v_exp_f32_e32 v91, v91
	v_add_f32_e32 v128, v87, v128
	v_exp_f32_e32 v92, v92
	v_add_f32_e32 v128, v88, v128
	v_exp_f32_e32 v93, v93
	v_add_f32_e32 v128, v89, v128
	v_exp_f32_e32 v94, v94
	v_add_f32_e32 v128, v90, v128
	v_exp_f32_e32 v95, v95
	v_add_f32_e32 v128, v91, v128
	v_add_f32_e32 v128, v92, v128
	v_add_f32_e32 v128, v93, v128
	v_add_f32_e32 v128, v94, v128
	v_add_f32_e32 v128, v95, v128
	v_mov_b32_e32 v129, v128
	v_cvt_pk_bf16_f32 v162, v96, v97
	v_cvt_pk_bf16_f32 v163, v98, v99
	v_permlane32_swap_b32_e32 v128, v129
	v_add_f32_e32 v128, v128, v129
	v_add_f32_e32 v159, v159, v128
	v_cvt_pk_bf16_f32 v164, v100, v101
	v_cvt_pk_bf16_f32 v165, v102, v103
	v_cvt_pk_bf16_f32 v166, v104, v105
	v_cvt_pk_bf16_f32 v167, v106, v107
	v_cvt_pk_bf16_f32 v168, v108, v109
	v_cvt_pk_bf16_f32 v169, v110, v111
	v_cvt_pk_bf16_f32 v132, v80, v81
	v_cvt_pk_bf16_f32 v133, v82, v83
	v_cvt_pk_bf16_f32 v134, v84, v85
	v_cvt_pk_bf16_f32 v135, v86, v87
	v_cvt_pk_bf16_f32 v128, v88, v89
	v_cvt_pk_bf16_f32 v129, v90, v91
	v_cvt_pk_bf16_f32 v130, v92, v93
	v_cvt_pk_bf16_f32 v131, v94, v95
	s_waitcnt lgkmcnt(0)
	s_barrier
; #define SBAR() __builtin_amdgcn_sched_barrier(0)
; #define LWN1(a) do { if constexpr (NW == 0) LW1(0, a); else if constexpr (NW == 1) LW1(1, a); else if constexpr (NW == 2) LW1(2, a); else if constexpr (NW == 3) LW1(3, a); else if constexpr (NW == 4) LW1(4, a); else if constexpr (NW == 5) LW1(5, a); else LW1(6, a); } while (0)
; #define LWN2(a, b) do { if constexpr (NW == 0) LW2(0, a, b); else if constexpr (NW == 1) LW2(1, a, b); else if constexpr (NW == 2) LW2(2, a, b); else if constexpr (NW == 3) LW2(3, a, b); else if constexpr (NW == 4) LW2(4, a, b); else if constexpr (NW == 5) LW2(5, a, b); else LW2(6, a, b); } while (0)
; template <int DQK, bool HASQK, bool HASPV, int J> ...
;     constexpr int NQS = HASQK ? 2 * (DQK / 16) : 0, NS = NQS + (HASPV ? 16 : 0);
;     if constexpr (J < NS) {
;         constexpr int rd1 = (J + 1 < NS) ? ((J + 1 < NQS) ? 1 : 2) : 0, rd2 = (J + 2 < NS) ? ((J + 2 < NQS) ? 1 : 2) : 0, rd3 = (J + 3 < NS) ? ((J + 3 < NQS) ? 1 : 2) : 0, NW = rd1 + rd2 + rd3;
;     ...
;         if constexpr (J < NQS) { constexpr int d0 = J >> 1, h = J & 1;
;             LWN1(kf[d0][h]); SBAR();
;             if constexpr (h == 0) p0 = __builtin_amdgcn_mfma_f32_32x32x16_bf16(kf[d0][0], qr[d0], (d0 == 0) ? negm : p0, 0, 0, 0);
;             else p1 = __builtin_amdgcn_mfma_f32_32x32x16_bf16(kf[d0][1], qr[d0], (d0 == 0) ? negm : p1, 0, 0, 0);
;         } else { constexpr int q = J - NQS, g = q >> 2, d = q & 3;
;             LWN2(vf[g][2 * d], vf[g][2 * d + 1]); SBAR();
;             o[d] = __builtin_amdgcn_mfma_f32_32x32x16_bf16(pa[g], (bf16x8){vf[g][2 * d][0], vf[g][2 * d][1], vf[g][2 * d][2], vf[g][2 * d][3], vf[g][2 * d + 1][0], vf[g][2 * d + 1][1], vf[g][2 * d + 1][2], vf[g][2 * d + 1][3]}, o[d], 0, 0, 0);
;         }
;     ...
;         SBAR();
;         slot_read<DQK, HASQK, HASPV, J + 4>(kf, vf, ka_, vb_);
;         SBAR();
;         slot_run<DQK, HASQK, HASPV, J + 1>(kf, vf, ka_, vb_, qr, p0, p1, negm, o, pa);
; template <int DQK, bool HASQK, bool HASPV>
; __device__ __forceinline__ void seg_m2(const int (&ka_)[4], int vb_, const bf16x8* qr, f32x16& p0, f32x16& p1, const float nm, f32x16 (&o)[4], bf16x8 pa0, bf16x8 pa1, bf16x8 pa2, bf16x8 pa3) {
;     ...
;     f32x16 negm;
; #pragma unroll
;     for (int r = 0; r < 16; ++r) negm[r] = nm;
;     asm volatile("" : "+v"(negm));
	s_cmp_lg_u32 s86, 0
	s_cselect_b32 s46, s87, 0x8000
	s_lshl_b32 s47, s86, 13
	v_add_u32_e32 v188, s46, v157
	ds_read_b64_tr_b16 v[170:171], v188 offset:0
	ds_read_b64_tr_b16 v[172:173], v188 offset:2048
	ds_read_b64_tr_b16 v[174:175], v188 offset:512
	ds_read_b64_tr_b16 v[176:177], v188 offset:2560
	ds_read_b64_tr_b16 v[178:179], v188 offset:1024
	ds_read_b64_tr_b16 v[180:181], v188 offset:3072
	ds_read_b64_tr_b16 v[182:183], v188 offset:1536
	ds_read_b64_tr_b16 v[184:185], v188 offset:3584
	s_waitcnt lgkmcnt(6)
	v_mfma_f32_32x32x16_bf16 v[64:79], v[162:165], v[170:173], v[64:79]
	ds_read_b64_tr_b16 v[170:171], v188 offset:4096
	ds_read_b64_tr_b16 v[172:173], v188 offset:6144
	v_add_u32_e32 v232, s47, v141
	v_xor_b32_e32 v80, 0x80000000, v158
	v_mov_b32_e32 v81, v80
	s_waitcnt lgkmcnt(6)
	v_mfma_f32_32x32x16_bf16 v[48:63], v[162:165], v[174:177], v[48:63]
	ds_read_b64_tr_b16 v[174:175], v188 offset:4608
	ds_read_b64_tr_b16 v[176:177], v188 offset:6656
	v_add_u32_e32 v233, s47, v143
	v_mov_b32_e32 v82, v80
	s_waitcnt lgkmcnt(6)
	v_mfma_f32_32x32x16_bf16 v[32:47], v[162:165], v[178:181], v[32:47]
	ds_read_b64_tr_b16 v[178:179], v188 offset:5120
	ds_read_b64_tr_b16 v[180:181], v188 offset:7168
	v_add_u32_e32 v186, s47, v160
	v_mov_b32_e32 v83, v80
	s_waitcnt lgkmcnt(6)
	v_mfma_f32_32x32x16_bf16 v[16:31], v[162:165], v[182:185], v[16:31]
	ds_read_b64_tr_b16 v[182:183], v188 offset:5632
	ds_read_b64_tr_b16 v[184:185], v188 offset:7680
	v_add_u32_e32 v187, s47, v161
	v_mov_b32_e32 v84, v80
	s_waitcnt lgkmcnt(6)
	v_mfma_f32_32x32x16_bf16 v[64:79], v[166:169], v[170:173], v[64:79]
	ds_read_b64_tr_b16 v[170:171], v188 offset:8192
	ds_read_b64_tr_b16 v[172:173], v188 offset:10240
	v_mov_b32_e32 v85, v80
	s_waitcnt lgkmcnt(6)
	v_mfma_f32_32x32x16_bf16 v[48:63], v[166:169], v[174:177], v[48:63]
	ds_read_b64_tr_b16 v[174:175], v188 offset:8704
	ds_read_b64_tr_b16 v[176:177], v188 offset:10752
	v_mov_b32_e32 v86, v80
	s_waitcnt lgkmcnt(6)
	v_mfma_f32_32x32x16_bf16 v[32:47], v[166:169], v[178:181], v[32:47]
	ds_read_b64_tr_b16 v[178:179], v188 offset:9216
	ds_read_b64_tr_b16 v[180:181], v188 offset:11264
	v_mov_b32_e32 v87, v80
	s_waitcnt lgkmcnt(6)
	v_mfma_f32_32x32x16_bf16 v[16:31], v[166:169], v[182:185], v[16:31]
	ds_read_b64_tr_b16 v[182:183], v188 offset:9728
	ds_read_b64_tr_b16 v[184:185], v188 offset:11776
	v_mov_b32_e32 v88, v80
	s_waitcnt lgkmcnt(6)
	v_mfma_f32_32x32x16_bf16 v[64:79], v[132:135], v[170:173], v[64:79]
	ds_read_b64_tr_b16 v[170:171], v188 offset:12288
	ds_read_b64_tr_b16 v[172:173], v188 offset:14336
	v_mov_b32_e32 v89, v80
	s_waitcnt lgkmcnt(6)
	v_mfma_f32_32x32x16_bf16 v[48:63], v[132:135], v[174:177], v[48:63]
	ds_read_b64_tr_b16 v[174:175], v188 offset:12800
	ds_read_b64_tr_b16 v[176:177], v188 offset:14848
	v_mov_b32_e32 v90, v80
	s_waitcnt lgkmcnt(6)
	v_mfma_f32_32x32x16_bf16 v[32:47], v[132:135], v[178:181], v[32:47]
	ds_read_b64_tr_b16 v[178:179], v188 offset:13312
	ds_read_b64_tr_b16 v[180:181], v188 offset:15360
	v_mov_b32_e32 v91, v80
	s_waitcnt lgkmcnt(6)
	v_mfma_f32_32x32x16_bf16 v[16:31], v[132:135], v[182:185], v[16:31]
	ds_read_b64_tr_b16 v[182:183], v188 offset:13824
	ds_read_b64_tr_b16 v[184:185], v188 offset:15872
	v_mov_b32_e32 v92, v80
	s_waitcnt lgkmcnt(6)
	v_mfma_f32_32x32x16_bf16 v[64:79], v[128:131], v[170:173], v[64:79]
	ds_read_b128 v[170:173], v232 offset:0
	v_mov_b32_e32 v93, v80
	s_waitcnt lgkmcnt(5)
	v_mfma_f32_32x32x16_bf16 v[48:63], v[128:131], v[174:177], v[48:63]
	ds_read_b128 v[174:177], v232 offset:4096
	v_mov_b32_e32 v94, v80
	s_waitcnt lgkmcnt(4)
	v_mfma_f32_32x32x16_bf16 v[32:47], v[128:131], v[178:181], v[32:47]
	ds_read_b128 v[178:181], v233 offset:0
	v_mov_b32_e32 v95, v80
	s_waitcnt lgkmcnt(3)
	v_mfma_f32_32x32x16_bf16 v[16:31], v[128:131], v[182:185], v[16:31]
	ds_read_b128 v[182:185], v233 offset:4096
	s_waitcnt lgkmcnt(3)
	v_mfma_f32_32x32x16_bf16 v[96:111], v[170:173], v[112:115], v[80:95]
	ds_read_b128 v[170:173], v186 offset:0
	s_waitcnt lgkmcnt(3)
	v_mfma_f32_32x32x16_bf16 v[80:95], v[174:177], v[112:115], v[80:95]
	ds_read_b128 v[174:177], v186 offset:4096
	s_waitcnt lgkmcnt(3)
	v_mfma_f32_32x32x16_bf16 v[96:111], v[178:181], v[116:119], v[96:111]
	ds_read_b128 v[178:181], v187 offset:0
	s_waitcnt lgkmcnt(3)
	v_mfma_f32_32x32x16_bf16 v[80:95], v[182:185], v[116:119], v[80:95]
	ds_read_b128 v[182:185], v187 offset:4096
	s_waitcnt lgkmcnt(3)
	v_mfma_f32_32x32x16_bf16 v[96:111], v[170:173], v[120:123], v[96:111]
	s_waitcnt lgkmcnt(2)
	v_mfma_f32_32x32x16_bf16 v[80:95], v[174:177], v[120:123], v[80:95]
	s_waitcnt lgkmcnt(1)
	v_mfma_f32_32x32x16_bf16 v[96:111], v[178:181], v[124:127], v[96:111]
	s_waitcnt lgkmcnt(0)
	v_mfma_f32_32x32x16_bf16 v[80:95], v[182:185], v[124:127], v[80:95]
	v_lshl_add_u64 v[144:145], v[144:145], 0, s[28:29]
	v_lshl_add_u64 v[146:147], v[146:147], 0, s[28:29]
	v_lshl_add_u64 v[148:149], v[148:149], 0, s[28:29]
	s_waitcnt vmcnt(0)
	s_add_u32 s44, s44, 0x10000
	s_waitcnt lgkmcnt(0)
	s_barrier
	s_addc_u32 s45, s45, 0
	s_cmp_eq_u32 s44, 0x7f0000
	s_cbranch_scc1 .LBB0_662
